# relu2
# speedup vs baseline: 1.0218x; 1.0143x over previous
.LBB1_12:
	s_and_b32 s12, s19, 1
	s_lshr_b32 s13, s19, 1
	s_add_i32 s16, s19, 1
	v_lshl_add_u32 v231, s13, 3, v221
	s_cmp_lg_u32 s19, 3
	s_cselect_b32 s17, s16, 3
	s_waitcnt lgkmcnt(2)
	v_lshlrev_b32_e32 v2, 7, v231
	s_lshl_b32 s14, s12, 6
	v_or3_b32 v160, v2, s14, v220
	s_waitcnt lgkmcnt(0)
	v_mov_b32_e32 v1, v220
	v_lshl_add_u64 v[2:3], v[160:161], 2, s[6:7]
	global_load_dword v232, v[2:3], off
	s_lshl_b32 s14, s17, 2
	s_and_b32 s14, s14, 24
	s_lshl_b32 s13, s13, 9
	v_lshrrev_b32_e32 v3, 5, v1
	s_cmp_eq_u32 s12, 0
	v_add_u32_e32 v2, s14, v221
	v_lshlrev_b32_e32 v206, 4, v3
	s_cselect_b64 s[14:15], -1, 0
	s_cmp_eq_u32 s12, 1
	v_add3_u32 v149, v228, s13, v206
	s_cselect_b64 s[12:13], -1, 0
	s_lshl_b32 s17, s17, 6
	s_and_b32 s17, s17, 64
	v_lshl_or_b32 v2, v2, 7, s17
	v_lshl_add_u32 v234, v1, 4, 0
	v_and_or_b32 v1, v1, 31, v2
	v_mul_lo_u32 v2, v1, 27
	v_add_u32_e32 v233, 0xc000, v234
	v_mad_u64_u32 v[204:205], s[20:21], v3, 14, v[2:3]
	v_add_u32_e32 v202, 13, v2
	s_waitcnt vmcnt(3)
	v_mul_f32_e32 v1, 0.15915494, v222
	v_cos_f32_e32 v2, v1
	v_sin_f32_e32 v1, v1
	v_add_f32_e32 v2, v2, v2
	v_cndmask_b32_e64 v3, v2, v1, s[0:1]
	v_mul_f32_e32 v1, v1, v2
	v_fma_f32 v2, v2, v2, -2.0
	v_cndmask_b32_e64 v4, v2, v1, s[0:1]
	v_mul_f32_e32 v207, v1, v2
	v_fma_f32 v208, v2, v2, -2.0
	v_mul_f32_e32 v2, 0.15915494, v182
	v_cvt_pk_fp8_f32 v131, v225, v3
	v_cos_f32_e32 v3, v2
	v_sin_f32_e32 v2, v2
	v_cndmask_b32_e64 v1, v208, v207, s[0:1]
	v_cvt_pk_fp8_f32 v131, v4, v1 op_sel:[0,0,1]
	v_add_f32_e32 v1, v3, v3
	v_cvt_pk_f16_f32 v1, v2, v1
	v_cvt_pk_fp8_f32 v128, v182, v0
	v_cvt_scalef32_pk_fp8_f16 v132, v1, 1.0
	v_pk_fma_f16 v1, v1, v1, -2.0 op_sel:[1,0,1] op_sel_hi:[1,1,0]
	v_mul_f32_e32 v0, 0.15915494, v0
	v_cvt_scalef32_pk_fp8_f16 v132, v1, 1.0 op_sel:[0,0,1]
	v_pk_fma_f16 v1, v1, v1, -2.0 op_sel:[0,1,1] op_sel_hi:[1,1,0]
	v_cos_f32_e32 v2, v0
	v_cvt_scalef32_pk_fp8_f16 v133, v1, 1.0
	v_pk_fma_f16 v1, v1, v1, -2.0 op_sel:[0,1,1] op_sel_hi:[1,1,0]
	v_sin_f32_e32 v0, v0
	v_cvt_scalef32_pk_fp8_f16 v133, v1, 1.0 op_sel:[0,0,1]
	v_pk_fma_f16 v1, v1, v1, -2.0 op_sel:[0,1,1] op_sel_hi:[1,1,0]
	s_nop 0
	v_cvt_scalef32_pk_fp8_f16 v134, v1, 1.0
	v_pk_fma_f16 v1, v1, v1, -2.0 op_sel:[0,1,1] op_sel_hi:[1,1,0]
	s_nop 0
	v_cvt_scalef32_pk_fp8_f16 v134, v1, 1.0 op_sel:[0,0,1]
	v_add_f32_e32 v1, v2, v2
	v_cvt_pk_f16_f32 v0, v0, v1
	v_cvt_scalef32_pk_fp8_f16 v135, v0, 1.0
	v_pk_fma_f16 v24, v0, v0, -2.0 op_sel:[1,0,1] op_sel_hi:[1,1,0]
	s_waitcnt vmcnt(2)
	v_mul_f32_e32 v0, 0.15915494, v224
	v_cos_f32_e32 v1, v0
	v_sin_f32_e32 v0, v0
	v_add_f32_e32 v1, v1, v1
	v_cndmask_b32_e64 v2, v1, v0, s[0:1]
	v_mul_f32_e32 v0, v0, v1
	v_fma_f32 v1, v1, v1, -2.0
	v_cndmask_b32_e64 v3, v1, v0, s[0:1]
	v_mul_f32_e32 v209, v0, v1
	v_fma_f32 v210, v1, v1, -2.0
	v_mul_f32_e32 v1, 0.15915494, v190
	s_waitcnt vmcnt(1)
	v_cvt_pk_fp8_f32 v19, v223, v2
	v_cos_f32_e32 v2, v1
	v_sin_f32_e32 v1, v1
	v_cndmask_b32_e64 v0, v210, v209, s[0:1]
	v_cvt_pk_fp8_f32 v19, v3, v0 op_sel:[0,0,1]
	v_add_f32_e32 v0, v2, v2
	v_cvt_pk_f16_f32 v0, v1, v0
	v_cvt_scalef32_pk_fp8_f16 v20, v0, 1.0
	v_pk_fma_f16 v0, v0, v0, -2.0 op_sel:[1,0,1] op_sel_hi:[1,1,0]
	v_mul_f32_e32 v1, 0.15915494, v191
	v_cvt_scalef32_pk_fp8_f16 v135, v24, 1.0 op_sel:[0,0,1]
	v_cvt_scalef32_pk_fp8_f16 v20, v0, 1.0 op_sel:[0,0,1]
	v_pk_fma_f16 v0, v0, v0, -2.0 op_sel:[0,1,1] op_sel_hi:[1,1,0]
	v_cos_f32_e32 v2, v1
	v_pk_fma_f16 v24, v24, v24, -2.0 op_sel:[0,1,1] op_sel_hi:[1,1,0]
	v_cvt_scalef32_pk_fp8_f16 v21, v0, 1.0
	v_pk_fma_f16 v0, v0, v0, -2.0 op_sel:[0,1,1] op_sel_hi:[1,1,0]
	v_sin_f32_e32 v1, v1
	v_pk_fma_f16 v35, v24, v24, -2.0 op_sel:[0,1,1] op_sel_hi:[1,1,0]
	v_cvt_pk_fp8_f32 v128, v25, v185 op_sel:[0,0,1]
	v_cvt_scalef32_pk_fp8_f16 v21, v0, 1.0 op_sel:[0,0,1]
	v_pk_fma_f16 v0, v0, v0, -2.0 op_sel:[0,1,1] op_sel_hi:[1,1,0]
	v_pk_fma_f16 v36, v35, v35, -2.0 op_sel:[0,1,1] op_sel_hi:[1,1,0]
	v_mul_f32_e32 v25, 0.15915494, v25
	v_cvt_pk_fp8_f32 v129, v198, v162
	v_cvt_pk_fp8_f32 v130, v178, v200
	v_cvt_pk_fp8_f32 v16, v190, v191
	v_cvt_pk_fp8_f32 v17, v194, v195
	v_cvt_pk_fp8_f32 v18, v186, v187
	v_cvt_scalef32_pk_fp8_f16 v22, v0, 1.0
	v_pk_fma_f16 v0, v0, v0, -2.0 op_sel:[0,1,1] op_sel_hi:[1,1,0]
	v_pk_fma_f16 v37, v36, v36, -2.0 op_sel:[0,1,1] op_sel_hi:[1,1,0]
	v_cvt_scalef32_pk_fp8_f16 v137, v36, 1.0
	v_cos_f32_e32 v36, v25
	v_cvt_scalef32_pk_fp8_f16 v22, v0, 1.0 op_sel:[0,0,1]
	v_add_f32_e32 v0, v2, v2
	v_sin_f32_e32 v25, v25
	v_cvt_pk_f16_f32 v0, v1, v0
	v_mov_b32_e32 v160, v204
	v_cvt_scalef32_pk_fp8_f16 v23, v0, 1.0
	v_pk_fma_f16 v34, v0, v0, -2.0 op_sel:[1,0,1] op_sel_hi:[1,1,0]
	ds_read_b128 v[26:29], v234
	ds_read_b128 v[30:33], v234 offset:1024
	ds_read_b128 v[8:11], v234 offset:2048
	ds_read_b128 v[12:15], v234 offset:3072
	ds_read_b128 v[0:3], v234 offset:4096
	ds_read_b128 v[4:7], v234 offset:5120
	ds_read_b128 v[152:155], v234 offset:6144
	ds_read_b128 v[156:159], v234 offset:7168
	ds_read_b128 v[96:99], v149
	ds_read_b128 v[100:103], v149 offset:32
	ds_read_b128 v[104:107], v149 offset:64
	ds_read_b128 v[108:111], v149 offset:96
	v_cvt_pk_fp8_f32 v129, v163, v201 op_sel:[0,0,1]
	v_cvt_pk_fp8_f32 v130, v179, v181 op_sel:[0,0,1]
	v_cvt_pk_fp8_f32 v16, v192, v193 op_sel:[0,0,1]
	v_cvt_pk_fp8_f32 v17, v196, v197 op_sel:[0,0,1]
	v_cvt_pk_fp8_f32 v18, v188, v189 op_sel:[0,0,1]
	v_cvt_scalef32_pk_fp8_f16 v136, v24, 1.0
	v_add_f32_e32 v24, v36, v36
	v_cvt_pk_f16_f32 v24, v25, v24
	v_pk_fma_f16 v25, v24, v24, -2.0 op_sel:[1,0,1] op_sel_hi:[1,1,0]
	v_cvt_scalef32_pk_fp8_f16 v138, v24, 1.0
	v_cvt_scalef32_pk_fp8_f16 v23, v34, 1.0 op_sel:[0,0,1]
	v_cvt_scalef32_pk_fp8_f16 v136, v35, 1.0 op_sel:[0,0,1]
	v_pk_fma_f16 v35, v25, v25, -2.0 op_sel:[0,1,1] op_sel_hi:[1,1,0]
	v_cvt_scalef32_pk_fp8_f16 v138, v25, 1.0 op_sel:[0,0,1]
	v_mul_f32_e32 v25, 0.15915494, v185
	s_waitcnt lgkmcnt(0)
	v_mfma_scale_f32_32x32x64_f8f6f4 v[112:127], v[26:33], v[16:23], v[96:111], v227, v226 op_sel_hi:[0,0,0]
	v_cvt_scalef32_pk_fp8_f16 v139, v35, 1.0
	v_pk_fma_f16 v35, v35, v35, -2.0 op_sel:[0,1,1] op_sel_hi:[1,1,0]
	s_nop 0
	v_pk_fma_f16 v24, v35, v35, -2.0 op_sel:[0,1,1] op_sel_hi:[1,1,0]
	ds_read_b128 v[64:67], v149 offset:128
	ds_read_b128 v[68:71], v149 offset:160
	ds_read_b128 v[72:75], v149 offset:192
	ds_read_b128 v[76:79], v149 offset:224
	v_cvt_scalef32_pk_fp8_f16 v140, v24, 1.0
	v_pk_fma_f16 v24, v24, v24, -2.0 op_sel:[0,1,1] op_sel_hi:[1,1,0]
	v_cvt_scalef32_pk_fp8_f16 v137, v37, 1.0 op_sel:[0,0,1]
	v_cvt_scalef32_pk_fp8_f16 v140, v24, 1.0 op_sel:[0,0,1]
	v_cvt_scalef32_pk_fp8_f16 v139, v35, 1.0 op_sel:[0,0,1]
	v_mfma_scale_f32_32x32x64_f8f6f4 v[96:111], v[26:33], v[128:135], v[96:111], v227, v226 op_sel_hi:[0,0,0]
	v_cos_f32_e32 v26, v25
	v_sin_f32_e32 v25, v25
	v_mul_f32_e32 v30, 0.15915494, v192
	v_mul_f32_e32 v31, 0.15915494, v193
	v_add_f32_e32 v24, v26, v26
	v_cvt_pk_f16_f32 v24, v25, v24
	v_cvt_scalef32_pk_fp8_f16 v141, v24, 1.0
	v_pk_fma_f16 v24, v24, v24, -2.0 op_sel:[1,0,1] op_sel_hi:[1,1,0]
	s_nop 0
	v_cvt_scalef32_pk_fp8_f16 v141, v24, 1.0 op_sel:[0,0,1]
	v_pk_fma_f16 v26, v24, v24, -2.0 op_sel:[0,1,1] op_sel_hi:[1,1,0]
	v_lshl_add_u64 v[24:25], v[160:161], 2, s[4:5]
	v_pk_fma_f16 v27, v26, v26, -2.0 op_sel:[0,1,1] op_sel_hi:[1,1,0]
	s_nop 0
	v_pk_fma_f16 v28, v27, v27, -2.0 op_sel:[0,1,1] op_sel_hi:[1,1,0]
	s_waitcnt lgkmcnt(0)
	v_mfma_scale_f32_32x32x64_f8f6f4 v[80:95], v[8:15], v[16:23], v[64:79], v227, v226 op_sel_hi:[0,0,0]
	global_load_dwordx4 v[182:185], v[24:25], off
	global_load_dwordx4 v[190:193], v[24:25], off offset:3456
	v_cos_f32_e32 v25, v31
	v_pk_fma_f16 v29, v28, v28, -2.0 op_sel:[0,1,1] op_sel_hi:[1,1,0]
	v_cvt_scalef32_pk_fp8_f16 v143, v28, 1.0
	v_cvt_scalef32_pk_fp8_f16 v142, v26, 1.0
	v_cvt_scalef32_pk_fp8_f16 v143, v29, 1.0 op_sel:[0,0,1]
	v_cvt_scalef32_pk_fp8_f16 v142, v27, 1.0 op_sel:[0,0,1]
	v_add_f32_e32 v150, v25, v25
	v_mfma_scale_f32_32x32x64_f8f6f4 v[64:79], v[8:15], v[128:135], v[64:79], v227, v226 op_sel_hi:[0,0,0]
	v_pk_fma_f16 v8, v34, v34, -2.0 op_sel:[0,1,1] op_sel_hi:[1,1,0]
	ds_read_b128 v[32:35], v149 offset:256
	ds_read_b128 v[36:39], v149 offset:288
	ds_read_b128 v[40:43], v149 offset:320
	ds_read_b128 v[44:47], v149 offset:352
	v_pk_fma_f16 v9, v8, v8, -2.0 op_sel:[0,1,1] op_sel_hi:[1,1,0]
	v_cvt_scalef32_pk_fp8_f16 v144, v8, 1.0
	v_pk_fma_f16 v10, v9, v9, -2.0 op_sel:[0,1,1] op_sel_hi:[1,1,0]
	v_cvt_scalef32_pk_fp8_f16 v144, v9, 1.0 op_sel:[0,0,1]
	v_pk_fma_f16 v11, v10, v10, -2.0 op_sel:[0,1,1] op_sel_hi:[1,1,0]
	v_cvt_scalef32_pk_fp8_f16 v145, v10, 1.0
	v_cos_f32_e32 v10, v30
	v_cvt_scalef32_pk_fp8_f16 v145, v11, 1.0 op_sel:[0,0,1]
	v_sin_f32_e32 v11, v30
	v_add_f32_e32 v8, v10, v10
	v_cvt_pk_f16_f32 v8, v11, v8
	v_pk_fma_f16 v9, v8, v8, -2.0 op_sel:[1,0,1] op_sel_hi:[1,1,0]
	v_cvt_scalef32_pk_fp8_f16 v146, v8, 1.0
	v_pk_fma_f16 v10, v9, v9, -2.0 op_sel:[0,1,1] op_sel_hi:[1,1,0]
	s_waitcnt lgkmcnt(0)
	v_mfma_scale_f32_32x32x64_f8f6f4 v[48:63], v[0:7], v[16:23], v[32:47], v227, v226 op_sel_hi:[0,0,0]
	v_cvt_scalef32_pk_fp8_f16 v147, v10, 1.0
	v_pk_fma_f16 v10, v10, v10, -2.0 op_sel:[0,1,1] op_sel_hi:[1,1,0]
	v_cvt_scalef32_pk_fp8_f16 v146, v9, 1.0 op_sel:[0,0,1]
	v_cvt_scalef32_pk_fp8_f16 v147, v10, 1.0 op_sel:[0,0,1]
	v_pk_fma_f16 v24, v10, v10, -2.0 op_sel:[0,1,1] op_sel_hi:[1,1,0]
	s_nop 0
	v_cvt_scalef32_pk_fp8_f16 v148, v24, 1.0
	v_pk_fma_f16 v24, v24, v24, -2.0 op_sel:[0,1,1] op_sel_hi:[1,1,0]
	s_nop 0
	v_cvt_scalef32_pk_fp8_f16 v148, v24, 1.0 op_sel:[0,0,1]
	v_mfma_scale_f32_32x32x64_f8f6f4 v[32:47], v[0:7], v[128:135], v[32:47], v227, v226 op_sel_hi:[0,0,0]
	ds_read_b128 v[0:3], v149 offset:384
	ds_read_b128 v[4:7], v149 offset:416
	ds_read_b128 v[8:11], v149 offset:448
	ds_read_b128 v[12:15], v149 offset:480
	v_sin_f32_e32 v149, v31
	s_nop 0
	v_cvt_pk_f16_f32 v150, v149, v150
	v_cvt_scalef32_pk_fp8_f16 v149, v150, 1.0
	v_pk_fma_f16 v150, v150, v150, -2.0 op_sel:[1,0,1] op_sel_hi:[1,1,0]
	s_nop 0
	v_pk_fma_f16 v160, v150, v150, -2.0 op_sel:[0,1,1] op_sel_hi:[1,1,0]
	v_cvt_scalef32_pk_fp8_f16 v149, v150, 1.0 op_sel:[0,0,1]
	v_pk_fma_f16 v164, v160, v160, -2.0 op_sel:[0,1,1] op_sel_hi:[1,1,0]
	s_nop 0
	v_pk_fma_f16 v150, v164, v164, -2.0 op_sel:[0,1,1] op_sel_hi:[1,1,0]
	s_waitcnt lgkmcnt(0)
	v_mfma_scale_f32_32x32x64_f8f6f4 v[16:31], v[152:159], v[16:23], v[0:15], v227, v226 op_sel_hi:[0,0,0]
	v_pk_fma_f16 v165, v150, v150, -2.0 op_sel:[0,1,1] op_sel_hi:[1,1,0]
	v_cvt_scalef32_pk_fp8_f16 v151, v150, 1.0
	v_cvt_scalef32_pk_fp8_f16 v150, v160, 1.0
	v_cvt_scalef32_pk_fp8_f16 v151, v165, 1.0 op_sel:[0,0,1]
	v_cvt_scalef32_pk_fp8_f16 v150, v164, 1.0 op_sel:[0,0,1]
	v_mfma_scale_f32_32x32x64_f8f6f4 v[0:15], v[152:159], v[128:135], v[0:15], v227, v226 op_sel_hi:[0,0,0]
	v_mul_f32_e32 v128, 0.15915494, v198
	v_cos_f32_e32 v129, v128
	v_sin_f32_e32 v128, v128
	v_mul_f32_e32 v133, 0.15915494, v162
	v_cos_f32_e32 v134, v133
	v_add_f32_e32 v129, v129, v129
	v_cvt_pk_f16_f32 v130, v128, v129
	v_pk_fma_f16 v131, v130, v130, -2.0 op_sel:[1,0,1] op_sel_hi:[1,1,0]
	v_sin_f32_e32 v133, v133
	v_pk_fma_f16 v128, v131, v131, -2.0 op_sel:[0,1,1] op_sel_hi:[1,1,0]
	s_nop 0
	v_pk_fma_f16 v132, v128, v128, -2.0 op_sel:[0,1,1] op_sel_hi:[1,1,0]
	v_cvt_scalef32_pk_fp8_f16 v129, v128, 1.0
	v_cvt_scalef32_pk_fp8_f16 v128, v130, 1.0
	v_add_f32_e32 v130, v134, v134
	v_cvt_scalef32_pk_fp8_f16 v128, v131, 1.0 op_sel:[0,0,1]
	v_cvt_pk_f16_f32 v130, v133, v130
	v_cvt_scalef32_pk_fp8_f16 v129, v132, 1.0 op_sel:[0,0,1]
	v_cvt_scalef32_pk_fp8_f16 v131, v130, 1.0
	v_pk_fma_f16 v133, v130, v130, -2.0 op_sel:[1,0,1] op_sel_hi:[1,1,0]
	v_pk_fma_f16 v132, v132, v132, -2.0 op_sel:[0,1,1] op_sel_hi:[1,1,0]
	ds_read_b128 v[152:155], v234 offset:8192
	ds_read_b128 v[156:159], v234 offset:9216
	ds_read_b128 v[164:167], v234 offset:10240
	ds_read_b128 v[168:171], v234 offset:11264
	ds_read_b128 v[236:239], v234 offset:12288
	ds_read_b128 v[240:243], v234 offset:13312
	v_cvt_scalef32_pk_fp8_f16 v130, v132, 1.0
	v_pk_fma_f16 v132, v132, v132, -2.0 op_sel:[0,1,1] op_sel_hi:[1,1,0]
	v_mul_f32_e32 v135, 0.15915494, v163
	s_waitcnt lgkmcnt(4)
	v_mfma_scale_f32_32x32x64_f8f6f4 v[96:111], v[152:159], v[136:143], v[96:111], v227, v226 op_sel_hi:[0,0,0]
	v_cvt_scalef32_pk_fp8_f16 v131, v133, 1.0 op_sel:[0,0,1]
	v_pk_fma_f16 v133, v133, v133, -2.0 op_sel:[0,1,1] op_sel_hi:[1,1,0]
	v_cvt_scalef32_pk_fp8_f16 v130, v132, 1.0 op_sel:[0,0,1]
	v_cvt_scalef32_pk_fp8_f16 v132, v133, 1.0
	v_pk_fma_f16 v133, v133, v133, -2.0 op_sel:[0,1,1] op_sel_hi:[1,1,0]
	ds_read_b128 v[244:247], v234 offset:14336
	ds_read_b128 v[248:251], v234 offset:15360
	v_pk_fma_f16 v134, v133, v133, -2.0 op_sel:[0,1,1] op_sel_hi:[1,1,0]
	v_cvt_scalef32_pk_fp8_f16 v132, v133, 1.0 op_sel:[0,0,1]
	v_cvt_scalef32_pk_fp8_f16 v133, v134, 1.0
	v_pk_fma_f16 v134, v134, v134, -2.0 op_sel:[0,1,1] op_sel_hi:[1,1,0]
	s_nop 0
	v_cvt_scalef32_pk_fp8_f16 v133, v134, 1.0 op_sel:[0,0,1]
	v_mfma_scale_f32_32x32x64_f8f6f4 v[112:127], v[152:159], v[144:151], v[112:127], v227, v226 op_sel_hi:[0,0,0]
	v_cos_f32_e32 v152, v135
	v_sin_f32_e32 v135, v135
	v_mul_f32_e32 v154, 0.15915494, v194
	v_cos_f32_e32 v155, v154
	v_add_f32_e32 v134, v152, v152
	v_cvt_pk_f16_f32 v152, v135, v134
	v_pk_fma_f16 v153, v152, v152, -2.0 op_sel:[1,0,1] op_sel_hi:[1,1,0]
	v_sin_f32_e32 v154, v154
	v_pk_fma_f16 v134, v153, v153, -2.0 op_sel:[0,1,1] op_sel_hi:[1,1,0]
	s_nop 0
	v_pk_fma_f16 v160, v134, v134, -2.0 op_sel:[0,1,1] op_sel_hi:[1,1,0]
	v_cvt_scalef32_pk_fp8_f16 v135, v134, 1.0
	v_cvt_scalef32_pk_fp8_f16 v134, v152, 1.0
	v_add_f32_e32 v152, v155, v155
	s_waitcnt lgkmcnt(4)
	v_mfma_scale_f32_32x32x64_f8f6f4 v[64:79], v[164:171], v[136:143], v[64:79], v227, v226 op_sel_hi:[0,0,0]
	v_mul_f32_e32 v157, 0.15915494, v195
	v_cvt_pk_f16_f32 v154, v154, v152
	v_cos_f32_e32 v158, v157
	v_pk_fma_f16 v155, v154, v154, -2.0 op_sel:[1,0,1] op_sel_hi:[1,1,0]
	v_sin_f32_e32 v157, v157
	v_pk_fma_f16 v152, v155, v155, -2.0 op_sel:[0,1,1] op_sel_hi:[1,1,0]
	v_cvt_scalef32_pk_fp8_f16 v134, v153, 1.0 op_sel:[0,0,1]
	v_pk_fma_f16 v156, v152, v152, -2.0 op_sel:[0,1,1] op_sel_hi:[1,1,0]
	v_cvt_scalef32_pk_fp8_f16 v153, v152, 1.0
	v_cvt_scalef32_pk_fp8_f16 v152, v154, 1.0
	v_add_f32_e32 v154, v158, v158
	v_mul_f32_e32 v159, 0.15915494, v196
	v_cvt_scalef32_pk_fp8_f16 v152, v155, 1.0 op_sel:[0,0,1]
	v_mfma_scale_f32_32x32x64_f8f6f4 v[80:95], v[164:171], v[144:151], v[80:95], v227, v226 op_sel_hi:[0,0,0]
	v_cvt_pk_f16_f32 v154, v157, v154
	v_cvt_scalef32_pk_fp8_f16 v153, v156, 1.0 op_sel:[0,0,1]
	v_cvt_scalef32_pk_fp8_f16 v155, v154, 1.0
	v_pk_fma_f16 v156, v156, v156, -2.0 op_sel:[0,1,1] op_sel_hi:[1,1,0]
	v_pk_fma_f16 v157, v154, v154, -2.0 op_sel:[1,0,1] op_sel_hi:[1,1,0]
	v_cvt_scalef32_pk_fp8_f16 v154, v156, 1.0
	v_pk_fma_f16 v156, v156, v156, -2.0 op_sel:[0,1,1] op_sel_hi:[1,1,0]
	v_cvt_scalef32_pk_fp8_f16 v155, v157, 1.0 op_sel:[0,0,1]
	v_pk_fma_f16 v157, v157, v157, -2.0 op_sel:[0,1,1] op_sel_hi:[1,1,0]
	v_cvt_scalef32_pk_fp8_f16 v154, v156, 1.0 op_sel:[0,0,1]
	v_cvt_scalef32_pk_fp8_f16 v156, v157, 1.0
	v_pk_fma_f16 v157, v157, v157, -2.0 op_sel:[0,1,1] op_sel_hi:[1,1,0]
	s_waitcnt lgkmcnt(0)
	v_mfma_scale_f32_32x32x64_f8f6f4 v[0:15], v[244:251], v[136:143], v[0:15], v227, v226 op_sel_hi:[0,0,0]
	v_cvt_scalef32_pk_fp8_f16 v156, v157, 1.0 op_sel:[0,0,1]
	v_pk_fma_f16 v158, v157, v157, -2.0 op_sel:[0,1,1] op_sel_hi:[1,1,0]
	v_cvt_scalef32_pk_fp8_f16 v135, v160, 1.0 op_sel:[0,0,1]
	v_cvt_scalef32_pk_fp8_f16 v157, v158, 1.0
	v_mfma_scale_f32_32x32x64_f8f6f4 v[32:47], v[236:243], v[136:143], v[32:47], v227, v226 op_sel_hi:[0,0,0]
	v_cos_f32_e32 v136, v159
	v_sin_f32_e32 v137, v159
	v_pk_fma_f16 v138, v158, v158, -2.0 op_sel:[0,1,1] op_sel_hi:[1,1,0]
	v_add_f32_e32 v136, v136, v136
	v_cvt_pk_f16_f32 v136, v137, v136
	v_pk_fma_f16 v137, v136, v136, -2.0 op_sel:[1,0,1] op_sel_hi:[1,1,0]
	v_cvt_scalef32_pk_fp8_f16 v157, v138, 1.0 op_sel:[0,0,1]
	v_pk_fma_f16 v138, v137, v137, -2.0 op_sel:[0,1,1] op_sel_hi:[1,1,0]
	s_nop 0
	v_pk_fma_f16 v180, v138, v138, -2.0 op_sel:[0,1,1] op_sel_hi:[1,1,0]
	v_cvt_scalef32_pk_fp8_f16 v159, v138, 1.0
	v_cvt_scalef32_pk_fp8_f16 v158, v136, 1.0
	v_cvt_scalef32_pk_fp8_f16 v159, v180, 1.0 op_sel:[0,0,1]
	v_cvt_scalef32_pk_fp8_f16 v158, v137, 1.0 op_sel:[0,0,1]
	v_mfma_scale_f32_32x32x64_f8f6f4 v[48:63], v[236:243], v[144:151], v[48:63], v227, v226 op_sel_hi:[0,0,0]
	v_mfma_scale_f32_32x32x64_f8f6f4 v[16:31], v[244:251], v[144:151], v[16:31], v227, v226 op_sel_hi:[0,0,0]
	ds_read_b128 v[140:143], v234 offset:16384
	ds_read_b128 v[144:147], v234 offset:17408
	ds_read_b128 v[236:239], v234 offset:18432
	ds_read_b128 v[240:243], v234 offset:19456
	ds_read_b128 v[170:173], v234 offset:20480
	ds_read_b128 v[174:177], v234 offset:21504
	s_waitcnt lgkmcnt(4)
	v_mfma_scale_f32_32x32x64_f8f6f4 v[96:111], v[140:147], v[128:135], v[96:111], v227, v226 op_sel_hi:[0,0,0]
	v_pk_fma_f16 v139, v160, v160, -2.0 op_sel:[0,1,1] op_sel_hi:[1,1,0]
	v_mov_b32_e32 v160, v204
	ds_read_b128 v[162:165], v234 offset:22528
	ds_read_b128 v[166:169], v234 offset:23552
	v_mul_f32_e32 v136, 0.15915494, v201
	v_cos_f32_e32 v137, v136
	v_sin_f32_e32 v136, v136
	v_mul_f32_e32 v150, 0.15915494, v186
	v_cos_f32_e32 v151, v150
	v_add_f32_e32 v137, v137, v137
	v_cvt_pk_f16_f32 v136, v136, v137
	v_pk_fma_f16 v138, v136, v136, -2.0 op_sel:[1,0,1] op_sel_hi:[1,1,0]
	v_cvt_scalef32_pk_fp8_f16 v137, v136, 1.0
	v_mfma_scale_f32_32x32x64_f8f6f4 v[112:127], v[140:147], v[152:159], v[112:127], v227, v226 op_sel_hi:[0,0,0]
	v_mul_f32_e32 v140, 0.15915494, v178
	v_cos_f32_e32 v141, v140
	v_sin_f32_e32 v140, v140
	v_mul_f32_e32 v143, 0.15915494, v200
	v_cos_f32_e32 v144, v143
	v_add_f32_e32 v141, v141, v141
	v_cvt_pk_f16_f32 v141, v140, v141
	v_sin_f32_e32 v143, v143
	v_cvt_scalef32_pk_fp8_f16 v140, v141, 1.0
	v_pk_fma_f16 v141, v141, v141, -2.0 op_sel:[1,0,1] op_sel_hi:[1,1,0]
	v_mul_f32_e32 v146, 0.15915494, v197
	v_pk_fma_f16 v142, v141, v141, -2.0 op_sel:[0,1,1] op_sel_hi:[1,1,0]
	v_cvt_scalef32_pk_fp8_f16 v140, v141, 1.0 op_sel:[0,0,1]
	v_cvt_scalef32_pk_fp8_f16 v141, v142, 1.0
	v_pk_fma_f16 v145, v142, v142, -2.0 op_sel:[0,1,1] op_sel_hi:[1,1,0]
	v_add_f32_e32 v142, v144, v144
	v_cvt_pk_f16_f32 v144, v143, v142
	v_lshl_add_u64 v[142:143], v[160:161], 2, s[4:5]
	global_load_dwordx4 v[198:201], v[142:143], off offset:16
	global_load_dwordx4 v[194:197], v[142:143], off offset:3472
	v_cvt_scalef32_pk_fp8_f16 v141, v145, 1.0 op_sel:[0,0,1]
	v_pk_fma_f16 v160, v144, v144, -2.0 op_sel:[1,0,1] op_sel_hi:[1,1,0]
	v_cvt_scalef32_pk_fp8_f16 v143, v144, 1.0
	v_pk_fma_f16 v144, v145, v145, -2.0 op_sel:[0,1,1] op_sel_hi:[1,1,0]
	v_cos_f32_e32 v145, v146
	v_sin_f32_e32 v146, v146
	v_pk_fma_f16 v148, v138, v138, -2.0 op_sel:[0,1,1] op_sel_hi:[1,1,0]
	v_cvt_scalef32_pk_fp8_f16 v136, v139, 1.0
	v_pk_fma_f16 v139, v139, v139, -2.0 op_sel:[0,1,1] op_sel_hi:[1,1,0]
	v_pk_fma_f16 v149, v148, v148, -2.0 op_sel:[0,1,1] op_sel_hi:[1,1,0]
	v_cvt_scalef32_pk_fp8_f16 v142, v144, 1.0
	v_pk_fma_f16 v144, v144, v144, -2.0 op_sel:[0,1,1] op_sel_hi:[1,1,0]
	v_cvt_scalef32_pk_fp8_f16 v137, v138, 1.0 op_sel:[0,0,1]
	v_cvt_scalef32_pk_fp8_f16 v136, v139, 1.0 op_sel:[0,0,1]
	v_pk_fma_f16 v138, v149, v149, -2.0 op_sel:[0,1,1] op_sel_hi:[1,1,0]
	v_cvt_scalef32_pk_fp8_f16 v142, v144, 1.0 op_sel:[0,0,1]
	v_add_f32_e32 v144, v145, v145
	v_cvt_scalef32_pk_fp8_f16 v139, v138, 1.0
	v_pk_fma_f16 v138, v138, v138, -2.0 op_sel:[0,1,1] op_sel_hi:[1,1,0]
	s_waitcnt lgkmcnt(4)
	v_mfma_scale_f32_32x32x64_f8f6f4 v[64:79], v[236:243], v[128:135], v[64:79], v227, v226 op_sel_hi:[0,0,0]
	v_cvt_pk_f16_f32 v144, v146, v144
	v_cvt_scalef32_pk_fp8_f16 v139, v138, 1.0 op_sel:[0,0,1]
	v_pk_fma_f16 v146, v144, v144, -2.0 op_sel:[1,0,1] op_sel_hi:[1,1,0]
	v_cvt_scalef32_pk_fp8_f16 v138, v148, 1.0
	v_cvt_scalef32_pk_fp8_f16 v145, v144, 1.0
	v_pk_fma_f16 v147, v180, v180, -2.0 op_sel:[0,1,1] op_sel_hi:[1,1,0]
	v_pk_fma_f16 v148, v146, v146, -2.0 op_sel:[0,1,1] op_sel_hi:[1,1,0]
	v_cvt_scalef32_pk_fp8_f16 v138, v149, 1.0 op_sel:[0,0,1]
	v_cvt_scalef32_pk_fp8_f16 v144, v147, 1.0
	v_pk_fma_f16 v147, v147, v147, -2.0 op_sel:[0,1,1] op_sel_hi:[1,1,0]
	v_pk_fma_f16 v149, v148, v148, -2.0 op_sel:[0,1,1] op_sel_hi:[1,1,0]
	v_cvt_scalef32_pk_fp8_f16 v145, v146, 1.0 op_sel:[0,0,1]
	v_mfma_scale_f32_32x32x64_f8f6f4 v[80:95], v[236:243], v[152:159], v[80:95], v227, v226 op_sel_hi:[0,0,0]
	v_pk_fma_f16 v146, v149, v149, -2.0 op_sel:[0,1,1] op_sel_hi:[1,1,0]
	v_cvt_scalef32_pk_fp8_f16 v144, v147, 1.0 op_sel:[0,0,1]
	v_cvt_scalef32_pk_fp8_f16 v147, v146, 1.0
	v_pk_fma_f16 v146, v146, v146, -2.0 op_sel:[0,1,1] op_sel_hi:[1,1,0]
	v_sin_f32_e32 v150, v150
	v_cvt_scalef32_pk_fp8_f16 v147, v146, 1.0 op_sel:[0,0,1]
	v_cvt_scalef32_pk_fp8_f16 v146, v148, 1.0
	v_add_f32_e32 v148, v151, v151
	v_mul_f32_e32 v151, 0.15915494, v187
	v_cvt_scalef32_pk_fp8_f16 v146, v149, 1.0 op_sel:[0,0,1]
	v_cvt_pk_f16_f32 v149, v150, v148
	v_cvt_scalef32_pk_fp8_f16 v148, v149, 1.0
	s_waitcnt lgkmcnt(0)
	v_mfma_scale_f32_32x32x64_f8f6f4 v[0:15], v[162:169], v[128:135], v[0:15], v227, v226 op_sel_hi:[0,0,0]
	v_pk_fma_f16 v149, v149, v149, -2.0 op_sel:[1,0,1] op_sel_hi:[1,1,0]
	v_cvt_scalef32_pk_fp8_f16 v143, v160, 1.0 op_sel:[0,0,1]
	v_pk_fma_f16 v150, v149, v149, -2.0 op_sel:[0,1,1] op_sel_hi:[1,1,0]
	v_cvt_scalef32_pk_fp8_f16 v148, v149, 1.0 op_sel:[0,0,1]
	v_cvt_scalef32_pk_fp8_f16 v149, v150, 1.0
	v_mfma_scale_f32_32x32x64_f8f6f4 v[32:47], v[170:177], v[128:135], v[32:47], v227, v226 op_sel_hi:[0,0,0]
	v_cos_f32_e32 v128, v151
	v_sin_f32_e32 v129, v151
	v_pk_fma_f16 v130, v150, v150, -2.0 op_sel:[0,1,1] op_sel_hi:[1,1,0]
	v_add_f32_e32 v128, v128, v128
	v_cvt_pk_f16_f32 v128, v129, v128
	v_pk_fma_f16 v203, v128, v128, -2.0 op_sel:[1,0,1] op_sel_hi:[1,1,0]
	v_cvt_scalef32_pk_fp8_f16 v151, v128, 1.0
	v_pk_fma_f16 v128, v130, v130, -2.0 op_sel:[0,1,1] op_sel_hi:[1,1,0]
	s_nop 0
	v_cvt_scalef32_pk_fp8_f16 v150, v128, 1.0
	v_pk_fma_f16 v128, v128, v128, -2.0 op_sel:[0,1,1] op_sel_hi:[1,1,0]
	v_cvt_scalef32_pk_fp8_f16 v149, v130, 1.0 op_sel:[0,0,1]
	v_cvt_scalef32_pk_fp8_f16 v151, v203, 1.0 op_sel:[0,0,1]
	v_cvt_scalef32_pk_fp8_f16 v150, v128, 1.0 op_sel:[0,0,1]
	v_mfma_scale_f32_32x32x64_f8f6f4 v[48:63], v[170:177], v[152:159], v[48:63], v227, v226 op_sel_hi:[0,0,0]
	v_mfma_scale_f32_32x32x64_f8f6f4 v[16:31], v[162:169], v[152:159], v[16:31], v227, v226 op_sel_hi:[0,0,0]
	v_pk_fma_f16 v130, v160, v160, -2.0 op_sel:[0,1,1] op_sel_hi:[1,1,0]
	s_nop 0
	v_pk_fma_f16 v131, v130, v130, -2.0 op_sel:[0,1,1] op_sel_hi:[1,1,0]
	ds_read_b128 v[152:155], v234 offset:24576
	ds_read_b128 v[156:159], v234 offset:25600
	ds_read_b128 v[162:165], v234 offset:26624
	ds_read_b128 v[166:169], v234 offset:27648
	v_pk_fma_f16 v128, v131, v131, -2.0 op_sel:[0,1,1] op_sel_hi:[1,1,0]
	v_mov_b32_e32 v160, v204
	v_pk_fma_f16 v132, v128, v128, -2.0 op_sel:[0,1,1] op_sel_hi:[1,1,0]
	v_cvt_scalef32_pk_fp8_f16 v129, v128, 1.0
	v_cvt_scalef32_pk_fp8_f16 v129, v132, 1.0 op_sel:[0,0,1]
	v_mul_f32_e32 v132, 0.15915494, v179
	v_sin_f32_e32 v133, v132
	v_cos_f32_e32 v132, v132
	v_cvt_scalef32_pk_fp8_f16 v128, v130, 1.0
	v_cvt_scalef32_pk_fp8_f16 v128, v131, 1.0 op_sel:[0,0,1]
	v_add_f32_e32 v130, v132, v132
	v_cvt_pk_f16_f32 v132, v133, v130
	v_pk_fma_f16 v133, v132, v132, -2.0 op_sel:[1,0,1] op_sel_hi:[1,1,0]
	s_nop 0
	v_pk_fma_f16 v130, v133, v133, -2.0 op_sel:[0,1,1] op_sel_hi:[1,1,0]
	s_waitcnt lgkmcnt(2)
	v_mfma_scale_f32_32x32x64_f8f6f4 v[96:111], v[152:159], v[136:143], v[96:111], v227, v226 op_sel_hi:[0,0,0]
	v_cvt_scalef32_pk_fp8_f16 v131, v130, 1.0
	v_pk_fma_f16 v134, v130, v130, -2.0 op_sel:[0,1,1] op_sel_hi:[1,1,0]
	v_cvt_scalef32_pk_fp8_f16 v130, v132, 1.0
	v_cvt_scalef32_pk_fp8_f16 v131, v134, 1.0 op_sel:[0,0,1]
	v_cvt_scalef32_pk_fp8_f16 v130, v133, 1.0 op_sel:[0,0,1]
	v_pk_fma_f16 v133, v134, v134, -2.0 op_sel:[0,1,1] op_sel_hi:[1,1,0]
	v_mul_f32_e32 v134, 0.15915494, v181
	v_cos_f32_e32 v135, v134
	v_sin_f32_e32 v134, v134
	v_cvt_scalef32_pk_fp8_f16 v132, v133, 1.0
	v_pk_fma_f16 v133, v133, v133, -2.0 op_sel:[0,1,1] op_sel_hi:[1,1,0]
	ds_read_b128 v[170:173], v234 offset:28672
	ds_read_b128 v[174:177], v234 offset:29696
	ds_read_b128 v[236:239], v234 offset:30720
	ds_read_b128 v[240:243], v234 offset:31744
	v_cvt_scalef32_pk_fp8_f16 v132, v133, 1.0 op_sel:[0,0,1]
	v_add_f32_e32 v133, v135, v135
	v_mfma_scale_f32_32x32x64_f8f6f4 v[112:127], v[152:159], v[144:151], v[112:127], v227, v226 op_sel_hi:[0,0,0]
	v_cvt_pk_f16_f32 v152, v134, v133
	v_mul_f32_e32 v153, 0.15915494, v188
	v_lshl_add_u64 v[134:135], v[160:161], 2, s[4:5]
	v_mul_f32_e32 v154, 0.15915494, v189
	global_load_dwordx4 v[178:181], v[134:135], off offset:32
	global_load_dwordx4 v[186:189], v[134:135], off offset:3488
	v_pk_fma_f16 v134, v152, v152, -2.0 op_sel:[1,0,1] op_sel_hi:[1,1,0]
	v_cvt_scalef32_pk_fp8_f16 v133, v152, 1.0
	v_pk_fma_f16 v152, v134, v134, -2.0 op_sel:[0,1,1] op_sel_hi:[1,1,0]
	v_cvt_scalef32_pk_fp8_f16 v133, v134, 1.0 op_sel:[0,0,1]
	v_pk_fma_f16 v155, v152, v152, -2.0 op_sel:[0,1,1] op_sel_hi:[1,1,0]
	s_nop 0
	v_pk_fma_f16 v134, v155, v155, -2.0 op_sel:[0,1,1] op_sel_hi:[1,1,0]
	s_nop 0
	v_pk_fma_f16 v156, v134, v134, -2.0 op_sel:[0,1,1] op_sel_hi:[1,1,0]
	v_cvt_scalef32_pk_fp8_f16 v135, v134, 1.0
	v_cvt_scalef32_pk_fp8_f16 v134, v152, 1.0
	v_pk_fma_f16 v152, v203, v203, -2.0 op_sel:[0,1,1] op_sel_hi:[1,1,0]
	v_cvt_scalef32_pk_fp8_f16 v134, v155, 1.0 op_sel:[0,0,1]
	v_pk_fma_f16 v155, v152, v152, -2.0 op_sel:[0,1,1] op_sel_hi:[1,1,0]
	s_waitcnt lgkmcnt(4)
	v_mfma_scale_f32_32x32x64_f8f6f4 v[64:79], v[162:169], v[136:143], v[64:79], v227, v226 op_sel_hi:[0,0,0]
	v_cvt_scalef32_pk_fp8_f16 v135, v156, 1.0 op_sel:[0,0,1]
	v_pk_fma_f16 v156, v155, v155, -2.0 op_sel:[0,1,1] op_sel_hi:[1,1,0]
	s_nop 0
	v_pk_fma_f16 v157, v156, v156, -2.0 op_sel:[0,1,1] op_sel_hi:[1,1,0]
	v_mfma_scale_f32_32x32x64_f8f6f4 v[80:95], v[162:169], v[144:151], v[80:95], v227, v226 op_sel_hi:[0,0,0]
	v_cvt_scalef32_pk_fp8_f16 v165, v156, 1.0
	v_cos_f32_e32 v156, v153
	v_sin_f32_e32 v153, v153
	v_cvt_scalef32_pk_fp8_f16 v164, v152, 1.0
	v_add_f32_e32 v152, v156, v156
	v_cvt_pk_f16_f32 v152, v153, v152
	v_pk_fma_f16 v153, v152, v152, -2.0 op_sel:[1,0,1] op_sel_hi:[1,1,0]
	v_cvt_scalef32_pk_fp8_f16 v166, v152, 1.0
	v_cvt_scalef32_pk_fp8_f16 v164, v155, 1.0 op_sel:[0,0,1]
	v_pk_fma_f16 v155, v153, v153, -2.0 op_sel:[0,1,1] op_sel_hi:[1,1,0]
	v_cvt_scalef32_pk_fp8_f16 v166, v153, 1.0 op_sel:[0,0,1]
	s_waitcnt lgkmcnt(0)
	v_mfma_scale_f32_32x32x64_f8f6f4 v[0:15], v[236:243], v[136:143], v[0:15], v227, v226 op_sel_hi:[0,0,0]
	v_cos_f32_e32 v153, v154
	v_cvt_scalef32_pk_fp8_f16 v167, v155, 1.0
	v_pk_fma_f16 v155, v155, v155, -2.0 op_sel:[0,1,1] op_sel_hi:[1,1,0]
	v_sin_f32_e32 v154, v154
	v_pk_fma_f16 v152, v155, v155, -2.0 op_sel:[0,1,1] op_sel_hi:[1,1,0]
	s_nop 0
	v_cvt_scalef32_pk_fp8_f16 v168, v152, 1.0
	v_pk_fma_f16 v152, v152, v152, -2.0 op_sel:[0,1,1] op_sel_hi:[1,1,0]
	s_nop 0
	v_cvt_scalef32_pk_fp8_f16 v168, v152, 1.0 op_sel:[0,0,1]
	v_add_f32_e32 v152, v153, v153
	v_cvt_scalef32_pk_fp8_f16 v165, v157, 1.0 op_sel:[0,0,1]
	v_cvt_scalef32_pk_fp8_f16 v167, v155, 1.0 op_sel:[0,0,1]
	v_mfma_scale_f32_32x32x64_f8f6f4 v[32:47], v[170:177], v[136:143], v[32:47], v227, v226 op_sel_hi:[0,0,0]
	v_cvt_pk_f16_f32 v136, v154, v152
	v_cvt_scalef32_pk_fp8_f16 v169, v136, 1.0
	v_pk_fma_f16 v136, v136, v136, -2.0 op_sel:[1,0,1] op_sel_hi:[1,1,0]
	s_nop 0
	v_cvt_scalef32_pk_fp8_f16 v169, v136, 1.0 op_sel:[0,0,1]
	v_pk_fma_f16 v136, v136, v136, -2.0 op_sel:[0,1,1] op_sel_hi:[1,1,0]
	s_nop 0
	v_pk_fma_f16 v137, v136, v136, -2.0 op_sel:[0,1,1] op_sel_hi:[1,1,0]
	s_nop 0
	v_pk_fma_f16 v138, v137, v137, -2.0 op_sel:[0,1,1] op_sel_hi:[1,1,0]
	s_nop 0
	v_pk_fma_f16 v139, v138, v138, -2.0 op_sel:[0,1,1] op_sel_hi:[1,1,0]
	v_mfma_scale_f32_32x32x64_f8f6f4 v[48:63], v[170:177], v[144:151], v[48:63], v227, v226 op_sel_hi:[0,0,0]
	v_cvt_scalef32_pk_fp8_f16 v171, v138, 1.0
	v_cvt_scalef32_pk_fp8_f16 v170, v136, 1.0
	v_cvt_scalef32_pk_fp8_f16 v171, v139, 1.0 op_sel:[0,0,1]
	v_cvt_scalef32_pk_fp8_f16 v170, v137, 1.0 op_sel:[0,0,1]
	v_mfma_scale_f32_32x32x64_f8f6f4 v[16:31], v[236:243], v[144:151], v[16:31], v227, v226 op_sel_hi:[0,0,0]
	v_mul_f32_e32 v152, 0.15915494, v225
	ds_read_b128 v[136:139], v234 offset:32768
	ds_read_b128 v[140:143], v234 offset:33792
	v_cos_f32_e32 v153, v152
	v_sin_f32_e32 v152, v152
	v_mov_b32_e32 v205, v161
	s_waitcnt lgkmcnt(0)
	v_mfma_scale_f32_32x32x64_f8f6f4 v[96:111], v[136:143], v[128:135], v[96:111], v227, v226 op_sel_hi:[0,0,0]
	v_add_f32_e32 v153, v153, v153
	v_cvt_pk_f16_f32 v158, v152, v153
	v_mov_b32_e32 v203, v161
	v_cndmask_b32_e64 v162, 0, v222, s[0:1]
	v_mul_f32_e32 v163, 0.15915494, v223
	v_pk_fma_f16 v159, v158, v158, -2.0 op_sel:[1,0,1] op_sel_hi:[1,1,0]
	v_cndmask_b32_e64 v172, 0, v224, s[0:1]
	v_pk_fma_f16 v156, v159, v159, -2.0 op_sel:[0,1,1] op_sel_hi:[1,1,0]
	s_nop 0
	v_pk_fma_f16 v160, v156, v156, -2.0 op_sel:[0,1,1] op_sel_hi:[1,1,0]
	v_cvt_scalef32_pk_fp8_f16 v157, v156, 1.0
	v_cvt_scalef32_pk_fp8_f16 v156, v158, 1.0
	v_cvt_scalef32_pk_fp8_f16 v156, v159, 1.0 op_sel:[0,0,1]
	v_mfma_scale_f32_32x32x64_f8f6f4 v[112:127], v[136:143], v[164:171], v[112:127], v227, v226 op_sel_hi:[0,0,0]
	ds_read_b128 v[136:139], v234 offset:34816
	ds_read_b128 v[140:143], v234 offset:35840
	ds_read_b128 v[144:147], v234 offset:36864
	ds_read_b128 v[148:151], v234 offset:37888
	ds_read_b128 v[236:239], v234 offset:38912
	ds_read_b128 v[240:243], v234 offset:39936
	v_lshl_add_u64 v[152:153], v[204:205], 2, s[4:5]
	v_lshl_add_u64 v[154:155], v[202:203], 2, s[4:5]
	global_load_dword v225, v[152:153], off offset:48
	global_load_dword v222, v[154:155], off
	global_load_dword v224, v[154:155], off offset:3456
	global_load_dword v223, v[152:153], off offset:3504
	v_cvt_scalef32_pk_fp8_f16 v157, v160, 1.0 op_sel:[0,0,1]
	s_waitcnt lgkmcnt(4)
	v_mfma_scale_f32_32x32x64_f8f6f4 v[64:79], v[136:143], v[128:135], v[64:79], v227, v226 op_sel_hi:[0,0,0]
	v_mfma_scale_f32_32x32x64_f8f6f4 v[80:95], v[136:143], v[164:171], v[80:95], v227, v226 op_sel_hi:[0,0,0]
	v_mul_f32_e32 v136, v207, v208
	v_fma_f32 v137, v208, v208, -2.0
	v_cndmask_b32_e64 v138, v137, v136, s[0:1]
	v_mul_f32_e32 v136, v136, v137
	v_fma_f32 v137, v137, v137, -2.0
	v_cndmask_b32_e64 v139, v137, v136, s[0:1]
	v_cvt_pk_fp8_f32 v159, v138, v139
	v_mul_f32_e32 v136, v136, v137
	v_fma_f32 v137, v137, v137, -2.0
	v_cndmask_b32_e64 v136, v137, v136, s[0:1]
	v_cvt_pk_fp8_f32 v159, v136, v162 op_sel:[0,0,1]
	v_pk_fma_f16 v136, v160, v160, -2.0 op_sel:[0,1,1] op_sel_hi:[1,1,0]
	v_mov_b32_e32 v160, v161
	v_pk_fma_f16 v137, v136, v136, -2.0 op_sel:[0,1,1] op_sel_hi:[1,1,0]
	v_cvt_scalef32_pk_fp8_f16 v158, v136, 1.0
	v_cos_f32_e32 v136, v163
	v_cvt_scalef32_pk_fp8_f16 v158, v137, 1.0 op_sel:[0,0,1]
	v_sin_f32_e32 v137, v163
	s_waitcnt lgkmcnt(0)
	v_mfma_scale_f32_32x32x64_f8f6f4 v[0:15], v[236:243], v[128:135], v[0:15], v227, v226 op_sel_hi:[0,0,0]
	v_add_f32_e32 v136, v136, v136
	v_mov_b32_e32 v162, v161
	v_cvt_pk_f16_f32 v138, v137, v136
	v_pk_fma_f16 v139, v138, v138, -2.0 op_sel:[1,0,1] op_sel_hi:[1,1,0]
	s_nop 0
	v_pk_fma_f16 v136, v139, v139, -2.0 op_sel:[0,1,1] op_sel_hi:[1,1,0]
	v_mov_b32_e32 v163, v161
	v_pk_fma_f16 v140, v136, v136, -2.0 op_sel:[0,1,1] op_sel_hi:[1,1,0]
	v_cvt_scalef32_pk_fp8_f16 v137, v136, 1.0
	v_cvt_scalef32_pk_fp8_f16 v136, v138, 1.0
	v_cvt_scalef32_pk_fp8_f16 v136, v139, 1.0 op_sel:[0,0,1]
	v_mul_f32_e32 v138, v209, v210
	v_fma_f32 v139, v210, v210, -2.0
	v_cndmask_b32_e64 v141, v139, v138, s[0:1]
	v_mul_f32_e32 v138, v138, v139
	v_fma_f32 v142, v139, v139, -2.0
	v_cndmask_b32_e64 v143, v142, v138, s[0:1]
	v_cvt_pk_fp8_f32 v139, v141, v143
	v_mfma_scale_f32_32x32x64_f8f6f4 v[32:47], v[144:151], v[128:135], v[32:47], v227, v226 op_sel_hi:[0,0,0]
	v_mul_f32_e32 v128, v138, v142
	v_fma_f32 v129, v142, v142, -2.0
	v_cndmask_b32_e64 v128, v129, v128, s[0:1]
	v_cvt_pk_fp8_f32 v139, v128, v172 op_sel:[0,0,1]
	v_pk_fma_f16 v128, v140, v140, -2.0 op_sel:[0,1,1] op_sel_hi:[1,1,0]
	s_nop 0
	v_cvt_scalef32_pk_fp8_f16 v138, v128, 1.0
	v_pk_fma_f16 v128, v128, v128, -2.0 op_sel:[0,1,1] op_sel_hi:[1,1,0]
	v_cvt_scalef32_pk_fp8_f16 v137, v140, 1.0 op_sel:[0,0,1]
	v_cvt_scalef32_pk_fp8_f16 v138, v128, 1.0 op_sel:[0,0,1]
	v_mov_b32_e32 v140, v161
	v_mov_b32_e32 v141, v161
	v_mov_b32_e32 v142, v161
	v_mov_b32_e32 v143, v161
	v_mfma_scale_f32_32x32x64_f8f6f4 v[48:63], v[144:151], v[164:171], v[48:63], v227, v226 op_sel_hi:[0,0,0]
	v_mfma_scale_f32_32x32x64_f8f6f4 v[16:31], v[236:243], v[164:171], v[16:31], v227, v226 op_sel_hi:[0,0,0]
	ds_read_b128 v[128:131], v234 offset:40960
	ds_read_b128 v[132:135], v234 offset:41984
	s_waitcnt lgkmcnt(0)
	v_mfma_scale_f32_32x32x64_f8f6f4 v[96:111], v[128:135], v[156:163], v[96:111], v227, v226 op_sel_hi:[0,0,0]
	v_mfma_scale_f32_32x32x64_f8f6f4 v[112:127], v[128:135], v[136:143], v[112:127], v227, v226 op_sel_hi:[0,0,0]
	ds_read_b128 v[128:131], v234 offset:43008
	ds_read_b128 v[132:135], v234 offset:44032
	s_waitcnt lgkmcnt(0)
	v_mfma_scale_f32_32x32x64_f8f6f4 v[64:79], v[128:135], v[156:163], v[64:79], v227, v226 op_sel_hi:[0,0,0]
	v_mfma_scale_f32_32x32x64_f8f6f4 v[80:95], v[128:135], v[136:143], v[80:95], v227, v226 op_sel_hi:[0,0,0]
	ds_read_b128 v[128:131], v234 offset:45056
	ds_read_b128 v[132:135], v234 offset:46080
	s_waitcnt lgkmcnt(0)
	v_mfma_scale_f32_32x32x64_f8f6f4 v[32:47], v[128:135], v[156:163], v[32:47], v227, v226 op_sel_hi:[0,0,0]
	v_mfma_scale_f32_32x32x64_f8f6f4 v[48:63], v[128:135], v[136:143], v[48:63], v227, v226 op_sel_hi:[0,0,0]
	ds_read_b128 v[128:131], v234 offset:47104
	ds_read_b128 v[132:135], v234 offset:48128
	ds_read_b128 v[174:177], v234 offset:49152
	ds_read_b128 v[208:211], v234 offset:50176
	ds_read_b128 v[212:215], v234 offset:53248
	ds_read_b128 v[236:239], v234 offset:54272
	s_waitcnt lgkmcnt(4)
	v_mfma_scale_f32_32x32x64_f8f6f4 v[0:15], v[128:135], v[156:163], v[0:15], v227, v226 op_sel_hi:[0,0,0]
	v_mfma_scale_f32_32x32x64_f8f6f4 v[16:31], v[128:135], v[136:143], v[16:31], v227, v226 op_sel_hi:[0,0,0]
	v_cvt_pk_bf16_f32 v162, v96, v97 clamp
	v_cvt_pk_bf16_f32 v163, v98, v99 clamp
	v_cvt_pk_bf16_f32 v164, v100, v101 clamp
	v_cvt_pk_bf16_f32 v165, v102, v103 clamp
	v_cvt_pk_bf16_f32 v166, v112, v113 clamp
	v_cvt_pk_bf16_f32 v167, v114, v115 clamp
	v_cvt_pk_bf16_f32 v168, v116, v117 clamp
	v_cvt_pk_bf16_f32 v169, v118, v119 clamp
	v_cvt_pk_bf16_f32 v170, v104, v105 clamp
	v_cvt_pk_bf16_f32 v171, v106, v107 clamp
	v_cvt_pk_bf16_f32 v172, v108, v109 clamp
	v_add_u32_e32 v128, 0, v206
	v_cvt_pk_bf16_f32 v173, v110, v111 clamp
	v_add_u32_e32 v235, 0x18000, v128
	v_cvt_pk_bf16_f32 v202, v120, v121 clamp
	ds_read_b128 v[128:131], v235
	ds_read_b128 v[132:135], v235 offset:32
	ds_read_b128 v[136:139], v235 offset:64
	ds_read_b128 v[140:143], v235 offset:96
	v_cvt_pk_bf16_f32 v203, v122, v123 clamp
	ds_read_b128 v[96:99], v235 offset:128
	ds_read_b128 v[100:103], v235 offset:160
	ds_read_b128 v[104:107], v235 offset:192
	ds_read_b128 v[108:111], v235 offset:224
	v_cvt_pk_bf16_f32 v204, v124, v125 clamp
	v_cvt_pk_bf16_f32 v64, v64, v65
	s_waitcnt lgkmcnt(4)
	v_mfma_f32_32x32x16_bf16 v[144:159], v[174:177], v[166:169], v[128:143]
	v_cvt_pk_bf16_f32 v205, v126, v127 clamp
	ds_read_b128 v[240:243], v234 offset:57344
	ds_read_b128 v[244:247], v234 offset:58368
	ds_read_b128 v[248:251], v234 offset:61440
	ds_read_b128 v[252:255], v234 offset:62464
	v_cvt_pk_bf16_f32 v65, v74, v75 clamp
	v_cndmask_b32_e64 v230, v230, 0, s[14:15]
	v_mfma_f32_32x32x16_bf16 v[128:143], v[174:177], v[162:165], v[128:143]
	v_pk_max_i16 v174, v64, 0
	v_cvt_pk_bf16_f32 v175, v66, v67 clamp
	v_cvt_pk_bf16_f32 v176, v68, v69 clamp
	v_cvt_pk_bf16_f32 v177, v70, v71 clamp
	s_waitcnt lgkmcnt(4)
	v_mfma_f32_32x32x16_bf16 v[112:127], v[208:211], v[166:169], v[96:111]
	v_cvt_pk_bf16_f32 v80, v80, v81 clamp
	v_cvt_pk_bf16_f32 v81, v82, v83 clamp
	v_cvt_pk_bf16_f32 v82, v84, v85 clamp
	v_cvt_pk_bf16_f32 v83, v86, v87 clamp
	v_mfma_f32_32x32x16_bf16 v[96:111], v[208:211], v[162:165], v[96:111]
	v_cvt_pk_bf16_f32 v64, v72, v73 clamp
	v_cvt_pk_bf16_f32 v66, v76, v77 clamp
	v_cvt_pk_bf16_f32 v67, v78, v79 clamp
	v_cvt_pk_bf16_f32 v68, v88, v89 clamp
	v_cvt_pk_bf16_f32 v69, v90, v91 clamp
	v_cvt_pk_bf16_f32 v70, v92, v93 clamp
	v_cvt_pk_bf16_f32 v71, v94, v95 clamp
	v_add_u32_e32 v160, 0x14000, v234
	v_mfma_f32_32x32x16_bf16 v[128:143], v[212:215], v[170:173], v[128:143]
	v_mfma_f32_32x32x16_bf16 v[144:159], v[212:215], v[202:205], v[144:159]
	v_mfma_f32_32x32x16_bf16 v[96:111], v[236:239], v[170:173], v[96:111]
	v_mfma_f32_32x32x16_bf16 v[112:127], v[236:239], v[202:205], v[112:127]
	v_cvt_pk_bf16_f32 v76, v32, v33 clamp
	v_cvt_pk_bf16_f32 v77, v34, v35 clamp
	v_cvt_pk_bf16_f32 v78, v36, v37 clamp
	v_cvt_pk_bf16_f32 v79, v38, v39 clamp
	v_cvt_pk_bf16_f32 v88, v48, v49 clamp
	v_cvt_pk_bf16_f32 v89, v50, v51 clamp
	v_cvt_pk_bf16_f32 v90, v52, v53 clamp
	v_cvt_pk_bf16_f32 v91, v54, v55 clamp
	s_waitcnt lgkmcnt(3)
	v_mfma_f32_32x32x16_bf16 v[128:143], v[240:243], v[174:177], v[128:143]
	v_cvt_pk_bf16_f32 v72, v40, v41 clamp
	v_cvt_pk_bf16_f32 v73, v42, v43 clamp
	v_cvt_pk_bf16_f32 v74, v44, v45 clamp
	v_mfma_f32_32x32x16_bf16 v[144:159], v[240:243], v[80:83], v[144:159]
	ds_read_b128 v[92:95], v233 offset:16384
	ds_read_b128 v[208:211], v233 offset:17408
	ds_read_b128 v[236:239], v233 offset:20480
	ds_read_b128 v[240:243], v233 offset:21504
	v_cvt_pk_bf16_f32 v75, v46, v47 clamp
	v_cvt_pk_bf16_f32 v84, v56, v57 clamp
	v_cvt_pk_bf16_f32 v85, v58, v59 clamp
	s_waitcnt lgkmcnt(6)
	v_mfma_f32_32x32x16_bf16 v[96:111], v[244:247], v[174:177], v[96:111]
	v_cvt_pk_bf16_f32 v86, v60, v61 clamp
	v_cvt_pk_bf16_f32 v87, v62, v63 clamp
	v_mfma_f32_32x32x16_bf16 v[112:127], v[244:247], v[80:83], v[112:127]
	s_waitcnt lgkmcnt(5)
	v_mfma_f32_32x32x16_bf16 v[128:143], v[248:251], v[64:67], v[128:143]
	v_mfma_f32_32x32x16_bf16 v[144:159], v[248:251], v[68:71], v[144:159]
	s_waitcnt lgkmcnt(4)
	v_mfma_f32_32x32x16_bf16 v[96:111], v[252:255], v[64:67], v[96:111]
	v_mfma_f32_32x32x16_bf16 v[112:127], v[252:255], v[68:71], v[112:127]
	v_cvt_pk_bf16_f32 v206, v0, v1 clamp
	v_cvt_pk_bf16_f32 v207, v2, v3 clamp
	s_waitcnt lgkmcnt(2)
	v_mfma_f32_32x32x16_bf16 v[96:111], v[208:211], v[76:79], v[96:111]
	ds_read_b128 v[32:35], v233 offset:24576
	ds_read_b128 v[36:39], v233 offset:25600
	ds_read_b128 v[40:43], v233 offset:28672
	ds_read_b128 v[44:47], v233 offset:29696
	v_mfma_f32_32x32x16_bf16 v[112:127], v[208:211], v[88:91], v[112:127]
	v_cvt_pk_bf16_f32 v208, v4, v5 clamp
	v_cvt_pk_bf16_f32 v209, v6, v7 clamp
	v_cvt_pk_bf16_f32 v214, v16, v17 clamp
	v_cvt_pk_bf16_f32 v215, v18, v19 clamp
	v_cvt_pk_bf16_f32 v216, v20, v21 clamp
	v_cvt_pk_bf16_f32 v217, v22, v23 clamp
	v_mfma_f32_32x32x16_bf16 v[128:143], v[92:95], v[76:79], v[128:143]
	v_mfma_f32_32x32x16_bf16 v[144:159], v[92:95], v[88:91], v[144:159]
	v_cvt_pk_bf16_f32 v92, v8, v9 clamp
	v_cvt_pk_bf16_f32 v93, v10, v11 clamp
	v_cvt_pk_bf16_f32 v94, v12, v13 clamp
	v_cvt_pk_bf16_f32 v95, v14, v15 clamp
	v_cvt_pk_bf16_f32 v210, v24, v25 clamp
	v_cvt_pk_bf16_f32 v211, v26, v27 clamp
	v_cvt_pk_bf16_f32 v212, v28, v29 clamp
	v_cvt_pk_bf16_f32 v213, v30, v31 clamp
	s_waitcnt lgkmcnt(5)
	v_mfma_f32_32x32x16_bf16 v[128:143], v[236:239], v[72:75], v[128:143]
	v_mfma_f32_32x32x16_bf16 v[144:159], v[236:239], v[84:87], v[144:159]
	s_waitcnt lgkmcnt(4)
	v_mfma_f32_32x32x16_bf16 v[96:111], v[240:243], v[72:75], v[96:111]
	v_mfma_f32_32x32x16_bf16 v[112:127], v[240:243], v[84:87], v[112:127]
	s_waitcnt lgkmcnt(3)
	v_mfma_f32_32x32x16_bf16 v[128:143], v[32:35], v[206:209], v[128:143]
	ds_read_b128 v[0:3], v234 offset:51200
	ds_read_b128 v[236:239], v234 offset:52224
	ds_read_b128 v[240:243], v234 offset:55296
	ds_read_b128 v[244:247], v234 offset:56320
	v_mfma_f32_32x32x16_bf16 v[144:159], v[32:35], v[214:217], v[144:159]
	s_waitcnt lgkmcnt(6)
	v_mfma_f32_32x32x16_bf16 v[96:111], v[36:39], v[206:209], v[96:111]
	v_mfma_f32_32x32x16_bf16 v[112:127], v[36:39], v[214:217], v[112:127]
	s_waitcnt lgkmcnt(5)
	v_mfma_f32_32x32x16_bf16 v[128:143], v[40:43], v[92:95], v[128:143]
	v_mfma_f32_32x32x16_bf16 v[144:159], v[40:43], v[210:213], v[144:159]
	s_waitcnt lgkmcnt(4)
	v_mfma_f32_32x32x16_bf16 v[96:111], v[44:47], v[92:95], v[96:111]
	v_mfma_f32_32x32x16_bf16 v[112:127], v[44:47], v[210:213], v[112:127]
	ds_read_b128 v[32:35], v235 offset:256
	ds_read_b128 v[36:39], v235 offset:288
	ds_read_b128 v[40:43], v235 offset:320
	ds_read_b128 v[44:47], v235 offset:352
	s_nop 3
	v_cvt_pk_bf16_f32 v128, v128, v129 clamp
	v_cvt_pk_bf16_f32 v129, v130, v131 clamp
	v_cvt_pk_bf16_f32 v130, v132, v133 clamp
	v_cvt_pk_bf16_f32 v131, v134, v135 clamp
	s_waitcnt lgkmcnt(0)
	v_mfma_f32_32x32x16_bf16 v[48:63], v[0:3], v[166:169], v[32:47]
	v_cvt_pk_bf16_f32 v132, v144, v145 clamp
	v_cvt_pk_bf16_f32 v133, v146, v147 clamp
	v_cvt_pk_bf16_f32 v134, v148, v149 clamp
	v_cvt_pk_bf16_f32 v135, v150, v151 clamp
	v_mfma_f32_32x32x16_bf16 v[32:47], v[0:3], v[162:165], v[32:47]
	ds_read_b128 v[0:3], v235 offset:384
	ds_read_b128 v[4:7], v235 offset:416
	ds_read_b128 v[8:11], v235 offset:448
	ds_read_b128 v[12:15], v235 offset:480
	s_waitcnt lgkmcnt(0)
	v_mfma_f32_32x32x16_bf16 v[16:31], v[236:239], v[166:169], v[0:15]
	v_mfma_f32_32x32x16_bf16 v[0:15], v[236:239], v[162:165], v[0:15]
	ds_read_b128 v[162:165], v234 offset:59392
	ds_read_b128 v[166:169], v234 offset:60416
	ds_read_b128 v[236:239], v234 offset:63488
	ds_read_b128 v[248:251], v234 offset:64512
	v_mfma_f32_32x32x16_bf16 v[0:15], v[244:247], v[170:173], v[0:15]
	v_mfma_f32_32x32x16_bf16 v[32:47], v[240:243], v[170:173], v[32:47]
	v_mfma_f32_32x32x16_bf16 v[48:63], v[240:243], v[202:205], v[48:63]
	v_mfma_f32_32x32x16_bf16 v[16:31], v[244:247], v[202:205], v[16:31]
	s_waitcnt lgkmcnt(2)
	v_mfma_f32_32x32x16_bf16 v[0:15], v[166:169], v[174:177], v[0:15]
	v_cvt_pk_bf16_f32 v136, v136, v137 clamp
	v_cvt_pk_bf16_f32 v137, v138, v139 clamp
	v_cvt_pk_bf16_f32 v138, v140, v141 clamp
	v_cvt_pk_bf16_f32 v139, v142, v143 clamp
	v_cvt_pk_bf16_f32 v140, v152, v153 clamp
	v_mfma_f32_32x32x16_bf16 v[32:47], v[162:165], v[174:177], v[32:47]
	v_mfma_f32_32x32x16_bf16 v[48:63], v[162:165], v[80:83], v[48:63]
	v_mfma_f32_32x32x16_bf16 v[16:31], v[166:169], v[80:83], v[16:31]
	ds_read_b128 v[80:83], v233 offset:18432
	ds_read_b128 v[144:147], v233 offset:19456
	ds_read_b128 v[148:151], v233 offset:22528
	ds_read_b128 v[162:165], v233 offset:23552
	s_waitcnt lgkmcnt(4)
	v_mfma_f32_32x32x16_bf16 v[0:15], v[248:251], v[64:67], v[0:15]
	v_mfma_f32_32x32x16_bf16 v[32:47], v[236:239], v[64:67], v[32:47]
	v_cvt_pk_bf16_f32 v141, v154, v155 clamp
	v_cvt_pk_bf16_f32 v142, v156, v157 clamp
	v_cvt_pk_bf16_f32 v143, v158, v159 clamp
	v_mfma_f32_32x32x16_bf16 v[48:63], v[236:239], v[68:71], v[48:63]
	v_mfma_f32_32x32x16_bf16 v[16:31], v[248:251], v[68:71], v[16:31]
	s_waitcnt lgkmcnt(2)
	v_mfma_f32_32x32x16_bf16 v[0:15], v[144:147], v[76:79], v[0:15]
	v_mfma_f32_32x32x16_bf16 v[32:47], v[80:83], v[76:79], v[32:47]
	v_mfma_f32_32x32x16_bf16 v[48:63], v[80:83], v[88:91], v[48:63]
	ds_read_b128 v[64:67], v233 offset:26624
	ds_read_b128 v[68:71], v233 offset:27648
	ds_read_b128 v[76:79], v233 offset:30720
	ds_read_b128 v[80:83], v233 offset:31744
	v_mfma_f32_32x32x16_bf16 v[16:31], v[144:147], v[88:91], v[16:31]
	v_cvt_pk_bf16_f32 v96, v96, v97 clamp
	v_cvt_pk_bf16_f32 v97, v98, v99 clamp
	v_cvt_pk_bf16_f32 v98, v100, v101 clamp
	v_cvt_pk_bf16_f32 v99, v102, v103 clamp
	s_waitcnt lgkmcnt(4)
	v_mfma_f32_32x32x16_bf16 v[0:15], v[162:165], v[72:75], v[0:15]
	v_cvt_pk_bf16_f32 v100, v112, v113 clamp
	v_mfma_f32_32x32x16_bf16 v[32:47], v[148:151], v[72:75], v[32:47]
	v_cvt_pk_bf16_f32 v101, v114, v115 clamp
	v_cvt_pk_bf16_f32 v102, v116, v117 clamp
	v_cvt_pk_bf16_f32 v103, v118, v119 clamp
	v_mfma_f32_32x32x16_bf16 v[48:63], v[148:151], v[84:87], v[48:63]
	v_mfma_f32_32x32x16_bf16 v[16:31], v[162:165], v[84:87], v[16:31]
	s_waitcnt lgkmcnt(2)
	v_mfma_f32_32x32x16_bf16 v[0:15], v[68:71], v[206:209], v[0:15]
	ds_read_b128 v[84:87], v160
	ds_read_b128 v[112:115], v160 offset:1024
	ds_read_b128 v[116:119], v160 offset:2048
	ds_read_b128 v[144:147], v160 offset:3072
	v_mfma_f32_32x32x16_bf16 v[32:47], v[64:67], v[206:209], v[32:47]
	v_mfma_f32_32x32x16_bf16 v[48:63], v[64:67], v[214:217], v[48:63]
	v_cvt_pk_bf16_f32 v104, v104, v105 clamp
	v_cvt_pk_bf16_f32 v105, v106, v107 clamp
	v_cvt_pk_bf16_f32 v106, v108, v109 clamp
	v_cvt_pk_bf16_f32 v107, v110, v111 clamp
	v_mfma_f32_32x32x16_bf16 v[16:31], v[68:71], v[214:217], v[16:31]
	v_cvt_pk_bf16_f32 v108, v120, v121 clamp
	v_cvt_pk_bf16_f32 v109, v122, v123 clamp
	v_cvt_pk_bf16_f32 v110, v124, v125 clamp
	s_waitcnt lgkmcnt(4)
	v_mfma_f32_32x32x16_bf16 v[0:15], v[80:83], v[92:95], v[0:15]
	v_cvt_pk_bf16_f32 v111, v126, v127 clamp
	v_mfma_f32_32x32x16_bf16 v[32:47], v[76:79], v[92:95], v[32:47]
	v_mfma_f32_32x32x16_bf16 v[48:63], v[76:79], v[210:213], v[48:63]
	v_mfma_f32_32x32x16_bf16 v[16:31], v[80:83], v[210:213], v[16:31]
	s_waitcnt lgkmcnt(3)
	v_mfma_f32_4x4x4_16b_bf16 v[64:67], v[84:85], v[128:129], 0
	v_mfma_f32_4x4x4_16b_bf16 v[68:71], v[86:87], v[130:131], 0
	s_nop 7
	v_cvt_pk_bf16_f32 v32, v32, v33 clamp
	v_cvt_pk_bf16_f32 v33, v34, v35 clamp
	v_cvt_pk_bf16_f32 v34, v36, v37 clamp
	v_cvt_pk_bf16_f32 v35, v38, v39 clamp
	v_mfma_f32_4x4x4_16b_bf16 v[80:83], v[84:85], v[132:133], 0
	v_mfma_f32_4x4x4_16b_bf16 v[88:91], v[86:87], v[134:135], 0
	v_cvt_pk_bf16_f32 v48, v48, v49 clamp
	v_cvt_pk_bf16_f32 v49, v50, v51 clamp
	v_cvt_pk_bf16_f32 v50, v52, v53 clamp
	v_cvt_pk_bf16_f32 v51, v54, v55 clamp
	s_waitcnt lgkmcnt(2)
	v_mfma_f32_4x4x4_16b_bf16 v[64:67], v[112:113], v[136:137], v[64:67]
	v_mfma_f32_4x4x4_16b_bf16 v[68:71], v[114:115], v[138:139], v[68:71]
	v_cvt_pk_bf16_f32 v40, v40, v41 clamp
	v_cvt_pk_bf16_f32 v41, v42, v43 clamp
	v_cvt_pk_bf16_f32 v42, v44, v45 clamp
	v_cvt_pk_bf16_f32 v43, v46, v47 clamp
	v_mfma_f32_4x4x4_16b_bf16 v[80:83], v[112:113], v[140:141], v[80:83]
	v_mfma_f32_4x4x4_16b_bf16 v[88:91], v[114:115], v[142:143], v[88:91]
	s_waitcnt lgkmcnt(1)
	v_mfma_f32_4x4x4_16b_bf16 v[64:67], v[116:117], v[96:97], v[64:67]
	v_mfma_f32_4x4x4_16b_bf16 v[68:71], v[118:119], v[98:99], v[68:71]
	ds_read_b128 v[36:39], v160 offset:4096
	ds_read_b128 v[96:99], v160 offset:5120
	v_cvt_pk_bf16_f32 v0, v0, v1 clamp
	v_cvt_pk_bf16_f32 v1, v2, v3 clamp
	v_cvt_pk_bf16_f32 v2, v4, v5 clamp
	v_cvt_pk_bf16_f32 v3, v6, v7 clamp
	v_mfma_f32_4x4x4_16b_bf16 v[80:83], v[116:117], v[100:101], v[80:83]
	v_mfma_f32_4x4x4_16b_bf16 v[88:91], v[118:119], v[102:103], v[88:91]
	ds_read_b128 v[4:7], v160 offset:7168
	v_cvt_pk_bf16_f32 v12, v12, v13
	v_cvt_pk_bf16_f32 v24, v24, v25
	v_cvt_pk_bf16_f32 v25, v26, v27
	s_waitcnt lgkmcnt(3)
	v_mfma_f32_4x4x4_16b_bf16 v[64:67], v[144:145], v[104:105], v[64:67]
	v_mfma_f32_4x4x4_16b_bf16 v[68:71], v[146:147], v[106:107], v[68:71]
	v_cndmask_b32_e64 v219, v219, 0, s[14:15]
	v_cndmask_b32_e64 v218, v218, 0, s[14:15]
	v_mfma_f32_4x4x4_16b_bf16 v[80:83], v[144:145], v[108:109], v[80:83]
	v_mfma_f32_4x4x4_16b_bf16 v[88:91], v[146:147], v[110:111], v[88:91]
	s_waitcnt lgkmcnt(2)
	v_mfma_f32_4x4x4_16b_bf16 v[64:67], v[36:37], v[32:33], v[64:67]
	v_mfma_f32_4x4x4_16b_bf16 v[68:71], v[38:39], v[34:35], v[68:71]
	v_cvt_pk_bf16_f32 v34, v20, v21
	v_cvt_pk_bf16_f32 v35, v22, v23
	ds_read_b128 v[20:23], v160 offset:6144
	v_cvt_pk_bf16_f32 v32, v16, v17
	v_cvt_pk_bf16_f32 v33, v18, v19
	v_cvt_pk_bf16_f32 v16, v56, v57 clamp
	v_cvt_pk_bf16_f32 v17, v58, v59 clamp
	v_mfma_f32_4x4x4_16b_bf16 v[80:83], v[36:37], v[48:49], v[80:83]
	v_mfma_f32_4x4x4_16b_bf16 v[88:91], v[38:39], v[50:51], v[88:91]
	v_cvt_pk_bf16_f32 v18, v60, v61 clamp
	v_cvt_pk_bf16_f32 v19, v62, v63 clamp
	s_waitcnt lgkmcnt(2)
	v_mfma_f32_4x4x4_16b_bf16 v[64:67], v[96:97], v[40:41], v[64:67]
	v_mfma_f32_4x4x4_16b_bf16 v[68:71], v[98:99], v[42:43], v[68:71]
	v_mfma_f32_4x4x4_16b_bf16 v[80:83], v[96:97], v[16:17], v[80:83]
	v_mfma_f32_4x4x4_16b_bf16 v[88:91], v[98:99], v[18:19], v[88:91]
	v_cvt_pk_bf16_f32 v16, v8, v9
	v_cvt_pk_bf16_f32 v17, v10, v11
	v_pk_max_i16 v8, v24, 0
	v_pk_max_i16 v9, v25, 0
	v_cvt_pk_bf16_f32 v10, v28, v29 clamp
	v_cvt_pk_bf16_f32 v11, v30, v31 clamp
	s_waitcnt lgkmcnt(0)
	v_mfma_f32_4x4x4_16b_bf16 v[64:67], v[20:21], v[0:1], v[64:67]
	v_mfma_f32_4x4x4_16b_bf16 v[68:71], v[22:23], v[2:3], v[68:71]
	v_pk_max_i16 v0, v32, 0
	v_pk_max_i16 v1, v33, 0
	v_pk_max_i16 v2, v34, 0
	v_pk_max_i16 v3, v35, 0
	s_nop 1
	v_mfma_f32_4x4x4_16b_bf16 v[80:83], v[20:21], v[0:1], v[80:83]
	v_mfma_f32_4x4x4_16b_bf16 v[88:91], v[22:23], v[2:3], v[88:91]
	v_pk_max_i16 v0, v16, 0
	v_pk_max_i16 v1, v17, 0
	v_pk_max_i16 v2, v12, 0
	v_cvt_pk_bf16_f32 v3, v14, v15 clamp
	s_nop 1
	v_mfma_f32_4x4x4_16b_bf16 v[64:67], v[4:5], v[0:1], v[64:67]
	v_mfma_f32_4x4x4_16b_bf16 v[68:71], v[6:7], v[2:3], v[68:71]
	v_mfma_f32_4x4x4_16b_bf16 v[80:83], v[4:5], v[8:9], v[80:83]
	v_mfma_f32_4x4x4_16b_bf16 v[88:91], v[6:7], v[10:11], v[88:91]
	s_waitcnt vmcnt(10)
	s_nop 3
	v_pk_add_f32 v[64:65], v[64:65], v[68:69]
	v_pk_add_f32 v[80:81], v[80:81], v[88:89]
	v_add_f32_e32 v66, v66, v70
	v_add_f32_e32 v82, v82, v90
	s_nop 1
	v_permlane32_swap_b32_e32 v64, v80
	v_permlane32_swap_b32_e32 v65, v81
	v_permlane32_swap_b32_e32 v66, v82
	s_nop 0
	v_add_f32_e32 v64, v64, v80
	v_add_f32_e32 v65, v65, v81
	v_add_f32_e32 v66, v66, v82
	v_add_f32_e32 v3, s10, v64
	v_add_f32_e32 v4, s11, v65
	v_add_f32_e32 v5, s18, v66
	v_mul_f32_e32 v3, 0xbfb8aa3b, v3
	v_mul_f32_e32 v4, 0xbfb8aa3b, v4
	v_mul_f32_e32 v5, 0xbfb8aa3b, v5
	v_exp_f32_e32 v3, v3
	v_exp_f32_e32 v4, v4
	v_exp_f32_e32 v5, v5
	v_add_f32_e32 v3, 1.0, v3
	v_add_f32_e32 v4, 1.0, v4
	v_add_f32_e32 v5, 1.0, v5
	v_rcp_f32_e32 v3, v3
	v_rcp_f32_e32 v4, v4
	v_rcp_f32_e32 v5, v5
	v_fmac_f32_e32 v218, v232, v3
	v_fmac_f32_e32 v219, v232, v4
	v_fmac_f32_e32 v230, v232, v5
	s_andn2_b64 vcc, exec, s[12:13]
	s_cbranch_vccnz .LBB1_6
	v_add_f32_dpp v218, v218, v218 row_shr:1 row_mask:0xf bank_mask:0xf bound_ctrl:1
	v_add_f32_dpp v219, v219, v219 row_shr:1 row_mask:0xf bank_mask:0xf bound_ctrl:1
	v_add_f32_dpp v230, v230, v230 row_shr:1 row_mask:0xf bank_mask:0xf bound_ctrl:1
	v_add_f32_dpp v218, v218, v218 row_shr:2 row_mask:0xf bank_mask:0xf bound_ctrl:1
	v_add_f32_dpp v219, v219, v219 row_shr:2 row_mask:0xf bank_mask:0xf bound_ctrl:1
	v_add_f32_dpp v230, v230, v230 row_shr:2 row_mask:0xf bank_mask:0xf bound_ctrl:1
	v_add_f32_dpp v218, v218, v218 row_shr:4 row_mask:0xf bank_mask:0xf bound_ctrl:1
	v_add_f32_dpp v219, v219, v219 row_shr:4 row_mask:0xf bank_mask:0xf bound_ctrl:1
	v_add_f32_dpp v230, v230, v230 row_shr:4 row_mask:0xf bank_mask:0xf bound_ctrl:1
	v_add_f32_dpp v218, v218, v218 row_shr:8 row_mask:0xf bank_mask:0xf bound_ctrl:1
	v_add_f32_dpp v219, v219, v219 row_shr:8 row_mask:0xf bank_mask:0xf bound_ctrl:1
	v_add_f32_dpp v230, v230, v230 row_shr:8 row_mask:0xf bank_mask:0xf bound_ctrl:1
	v_mov_b32_e32 v0, 0
	v_mov_b32_e32 v1, 0
	v_mov_b32_e32 v5, 0
	v_mov_b32_dpp v0, v218 row_bcast:15 row_mask:0xa bank_mask:0xf
	v_mov_b32_dpp v1, v219 row_bcast:15 row_mask:0xa bank_mask:0xf
	v_mov_b32_dpp v5, v230 row_bcast:15 row_mask:0xa bank_mask:0xf
	v_lshl_add_u32 v6, v231, 1, v231
	v_ashrrev_i32_e32 v7, 31, v6
	v_add_f32_e32 v218, v218, v0
	v_add_f32_e32 v219, v219, v1
	v_add_f32_e32 v230, v230, v5
	v_mov_b32_e32 v0, 0
	v_mov_b32_e32 v1, 0
	v_mov_b32_e32 v5, 0
	v_mov_b32_dpp v0, v218 row_bcast:31 row_mask:0xc bank_mask:0xf
	v_mov_b32_dpp v1, v219 row_bcast:31 row_mask:0xc bank_mask:0xf
	v_mov_b32_dpp v5, v230 row_bcast:31 row_mask:0xc bank_mask:0xf
	v_lshl_add_u64 v[6:7], v[6:7], 2, s[8:9]
	v_cmp_eq_u32_e32 vcc, 63, v220
	v_add_f32_e32 v2, v218, v0
	v_add_f32_e32 v3, v219, v1
	v_add_f32_e32 v4, v230, v5
	s_and_saveexec_b64 s[12:13], vcc
	global_store_dwordx3 v[6:7], v[2:4], off
	s_branch .LBB1_5
